# MoE gate/up GEMM main loop on LDS-DMA staging (gathered A row offsets redistributed through a small LDS table)
# speedup vs baseline: 1.0392x; 1.0131x over previous
;     ...
;     for (int i = 0; i < 4; ++i) ao[i] = arow((tid >> 3) + 32 * i) + (tid & 7) * 8;
;     const int bk = tid >> 4, bnc = tid & 15;
;     constexpr int NRB = B_F32 ? 8 : 4;
;     u32x4 ra0[4], ra1[4]; u32x4 rb0[NRB], rb1[NRB];
;     auto gloadA = [&](int kt, u32x4 (&ra)[4]) __attribute__((always_inline)) {
; #pragma unroll
;         for (int i = 0; i < 4; ++i) ra[i] = *(const u32x4*)(Abase + (ao[i] + kt * 64));
;     };
;     auto gloadB = [&](int kt, u32x4 (&rb)[NRB]) __attribute__((always_inline)) {
;         if (B_F32) {
;             const float* bp = (const float*)Bbase + (boff + (unsigned)((kt * 64 + bk) * ldb));
; #pragma unroll
;             for (int i = 0; i < 4; ++i) {
;                 if (bval) { rb[2 * i] = *(const u32x4*)(bp + (unsigned)(16 * i * ldb)); rb[2 * i + 1] = *(const u32x4*)(bp + (unsigned)(16 * i * ldb) + 4); }
;                 else { rb[2 * i] = (u32x4){0u, 0u, 0u, 0u}; rb[2 * i + 1] = rb[2 * i]; }
;             }
;         } else {
;             const bf16* bp = (const bf16*)Bbase + (boff + (unsigned)((kt * 64 + bk) * ldb));
; #pragma unroll
;             for (int i = 0; i < 4; ++i) rb[i] = bval ? *(const u32x4*)(bp + (unsigned)(16 * i * ldb)) : (u32x4){0u, 0u, 0u, 0u};
;         }
;     };
;     auto lstore = [&](const u32x4 (&ra)[4], const u32x4 (&rb)[NRB]) __attribute__((always_inline)) {
; #pragma unroll
;         for (int i = 0; i < 4; ++i) { const int row = (tid >> 3) + 32 * i, kc = tid & 7;
;             const u32x4 v = (kc & 1) ? (u32x4){ra[i][2], ra[i][3], ra[i][0], ra[i][1]} : ra[i];
;             *(u32x4*)(lds + (kc >> 2) * GA_KH + row * 64 + (kc & 3) * 16) = v; }
; #pragma unroll
;         for (int i = 0; i < 4; ++i) { const int k = bk + 16 * i;
;             u32x4 v;
;             if (B_F32) { const f32x4 x = __builtin_bit_cast(f32x4, rb[2 * i]), y = __builtin_bit_cast(f32x4, rb[2 * i + 1]);
;                 v[0] = pk2bf(x[0], x[1]); v[1] = pk2bf(x[2], x[3]); v[2] = pk2bf(y[0], y[1]); v[3] = pk2bf(y[2], y[3]); }
;             else v = rb[i];
;             *(u32x4*)(lds + GB_OFF + k * GB_ST + bnc * 16) = v; }
;     };
;     const lds_cptr la = (lds_cptr)lds + (wr * 64 + fr) * 64 + fq * 16;
;     const lds_cptr lb = (lds_cptr)lds + GB_OFF + (8 * fq + (fr >> 2) + (fq & 1) * 4) * GB_ST + wc * 128 + (fr & 3) * 8;
;     const int bsw = (fq & 1) ? -4 * GB_ST : 4 * GB_ST;
.LBB0_162:
	s_and_b32 s7, s58, 7
	s_and_b32 s6, s59, 7
	s_lshl_b32 s15, s7, 7
	v_ashrrev_i32_e32 v4, 3, v118
	s_add_u32 s28, s42, 0x45c6000
	v_add_u32_e32 v4, v2, v4
	s_addc_u32 s29, s43, 0
	s_mul_i32 s7, s18, 0x11000
	v_cmp_lt_i32_e32 vcc, v4, v5
	v_add_u32_e32 v8, 32, v4
	s_add_u32 s7, s42, s7
	v_cndmask_b32_e32 v6, v2, v4, vcc
	v_cmp_lt_i32_e32 vcc, v8, v5
	v_add_u32_e32 v10, 64, v4
	s_addc_u32 s19, s43, 0
	v_cndmask_b32_e32 v8, v2, v8, vcc
	v_cmp_lt_i32_e32 vcc, v10, v5
	v_add_u32_e32 v4, 0x60, v4
	s_add_u32 s44, s7, 0x1012c000
	v_cndmask_b32_e32 v10, v2, v10, vcc
	v_cmp_lt_i32_e32 vcc, v4, v5
	s_addc_u32 s45, s19, 0
	v_ashrrev_i32_e32 v7, 31, v6
	v_cndmask_b32_e32 v4, v2, v4, vcc
	v_lshl_add_u64 v[6:7], v[6:7], 2, s[44:45]
	v_ashrrev_i32_e32 v9, 31, v8
	v_ashrrev_i32_e32 v11, 31, v10
	v_ashrrev_i32_e32 v5, 31, v4
	v_lshl_add_u64 v[8:9], v[8:9], 2, s[44:45]
	v_lshl_add_u64 v[10:11], v[10:11], 2, s[44:45]
	v_lshl_add_u64 v[4:5], v[4:5], 2, s[44:45]
	global_load_dword v12, v[6:7], off
	global_load_dword v13, v[8:9], off
	global_load_dword v14, v[10:11], off
	global_load_dword v15, v[4:5], off
	s_lshl_b32 s18, s18, 21
	v_bfe_u32 v2, v118, 4, 2
	v_ashrrev_i32_e32 v4, 1, v118
	v_bfe_u32 v6, v118, 4, 1
	s_add_u32 s18, s42, s18
	v_bfe_u32 v5, v118, 2, 2
	v_lshlrev_b32_e32 v7, 1, v118
	v_and_b32_e32 v120, 0xffffffc0, v4
	v_lshlrev_b32_e32 v19, 4, v2
	v_lshlrev_b32_e32 v2, 3, v2
	v_lshlrev_b32_e32 v4, 2, v6
	s_addc_u32 s19, s43, 0
	v_lshlrev_b32_e32 v16, 3, v118
	v_ashrrev_i32_e32 v17, 4, v118
	v_and_b32_e32 v7, 0x80, v7
	v_or3_b32 v2, v2, v5, v4
	s_movk_i32 s48, 0x120
	s_add_u32 s44, s18, 0x18dd5100
	v_and_b32_e32 v18, 0x78, v16
	v_lshlrev_b32_e32 v21, 10, v17
	v_mad_u32_u24 v2, v2, s48, v7
	s_addc_u32 s45, s19, 0
	s_lshl_b32 s18, s6, 7
	v_and_b32_e32 v119, 15, v118
	v_and_or_b32 v122, v16, 24, v2
	v_or3_b32 v2, v18, s18, v21
	v_cmp_eq_u32_e32 vcc, 0, v6
	v_or_b32_e32 v6, v120, v119
	v_lshl_add_u64 v[4:5], v[2:3], 1, s[44:45]
	v_cndmask_b32_e32 v20, v236, v237, vcc
	v_lshlrev_b32_e32 v22, 6, v6
	v_add_co_u32_e32 v6, vcc, s40, v4
	s_mov_b32 s18, 0x10000
	s_nop 0
	v_addc_co_u32_e32 v7, vcc, 0, v5, vcc
	v_add_co_u32_e32 v8, vcc, s18, v4
	s_mov_b32 s19, 0x18000
	s_nop 0
	v_addc_co_u32_e32 v9, vcc, 0, v5, vcc
	v_and_b32_e32 v121, 56, v16
	v_add_co_u32_e32 v10, vcc, s19, v4
	v_add_u32_e32 v2, 0x10000, v2
	s_nop 0
	v_addc_co_u32_e32 v11, vcc, 0, v5, vcc
	v_mov_b32_e32 v5, v3
	v_mov_b32_e32 v7, v3
	v_mov_b32_e32 v9, v3
	v_mov_b32_e32 v11, v3
	s_mov_b32 s7, 0
	v_add_u32_e32 v129, v22, v19
	v_add_u32_e32 v130, v122, v20
	s_waitcnt vmcnt(0)
	v_lshlrev_b32_e32 v123, 10, v12
	v_lshlrev_b32_e32 v124, 10, v13
	v_lshlrev_b32_e32 v125, 10, v14
	v_or_b32_e32 v4, v123, v121
	v_lshlrev_b32_e32 v126, 10, v15
	v_or_b32_e32 v6, v124, v121
	v_or_b32_e32 v8, v125, v121
	v_lshl_add_u64 v[4:5], v[4:5], 1, s[28:29]
	v_or_b32_e32 v10, v126, v121
	v_lshl_add_u64 v[6:7], v[6:7], 1, s[28:29]
	v_lshl_add_u64 v[4:5], v[8:9], 1, s[28:29]
	v_lshl_add_u64 v[6:7], v[10:11], 1, s[28:29]
	v_lshl_add_u64 v[4:5], v[2:3], 1, s[44:45]
	v_add_co_u32_e32 v6, vcc, s40, v4
	v_and_b32_e32 v2, 1, v118
	s_nop 0
	v_addc_co_u32_e32 v7, vcc, 0, v5, vcc
	v_add_co_u32_e32 v6, vcc, s18, v4
	v_cmp_eq_u32_e64 s[46:47], 0, v2
	s_nop 0
	v_addc_co_u32_e32 v7, vcc, 0, v5, vcc
	v_add_co_u32_e32 v4, vcc, s19, v4
	v_bfe_i32 v2, v118, 2, 1
	s_nop 0
	v_addc_co_u32_e32 v5, vcc, 0, v5, vcc
	v_and_b32_e32 v2, 0x2040, v2
	v_and_b32_e32 v4, 0xffffffc0, v16
	v_add_u32_e32 v2, v2, v4
	v_lshlrev_b32_e32 v4, 4, v118
	v_and_b32_e32 v5, 48, v4
	v_or3_b32 v4, v21, s15, v18
	v_mul_lo_u32 v6, v17, s48
	v_lshlrev_b32_e32 v7, 4, v119
	v_add_u32_e32 v116, 0x30000, v4
	v_mov_b32_e32 v4, 0
	v_add_u32_e32 v127, v2, v5
	v_add_u32_e32 v128, v6, v7
	s_lshl_b32 s48, s6, 8
	v_lshrrev_b32_e32 v116, 6, v118
	v_lshlrev_b32_e32 v116, 4, v116
	v_bfe_u32 v117, v118, 4, 2
	v_add_u32_e32 v116, v116, v117
	v_mul_u32_u24_e32 v116, 0x800, v116
	v_add_u32_e32 v116, s48, v116
	v_bfe_u32 v68, v118, 1, 3
	v_xor_b32_e32 v68, v68, v117
	v_lshlrev_b32_e32 v68, 1, v68
	v_and_b32_e32 v117, 1, v118
	v_or_b32_e32 v68, v68, v117
	v_lshl_add_u32 v214, v68, 4, v116
	v_add_u32_e32 v215, 0x2000, v214
	v_xor_b32_e32 v68, 8, v68
	v_lshl_add_u32 v216, v68, 4, v116
	v_add_u32_e32 v216, 0x4000, v216
	v_add_u32_e32 v217, 0x2000, v216
	v_lshrrev_b32_e32 v116, 3, v118
	v_lshlrev_b32_e32 v116, 2, v116
	s_barrier
	ds_write_b32 v116, v123 offset:36864
	ds_write_b32 v116, v124 offset:36992
	ds_write_b32 v116, v125 offset:37120
	ds_write_b32 v116, v126 offset:37248
	s_waitcnt lgkmcnt(0)
	s_barrier
	v_lshrrev_b32_e32 v117, 6, v118
	v_lshlrev_b32_e32 v117, 5, v117
	v_bfe_u32 v68, v118, 2, 4
	v_add_u32_e32 v117, v117, v68
	v_lshlrev_b32_e32 v117, 2, v117
	ds_read_b32 v123, v117 offset:36864
	ds_read_b32 v125, v117 offset:36928
	v_bfe_u32 v68, v118, 4, 2
	v_sub_u32_e32 v68, 0, v68
	v_and_b32_e32 v68, 3, v68
	v_and_b32_e32 v116, 3, v118
	v_xor_b32_e32 v68, v68, v116
	v_lshlrev_b32_e32 v68, 4, v68
	s_waitcnt lgkmcnt(0)
	v_lshl_add_u32 v123, v123, 1, v68
	v_add_u32_e32 v124, 64, v123
	v_lshl_add_u32 v125, v125, 1, v68
	v_add_u32_e32 v126, 64, v125
	v_bfe_u32 v116, v118, 2, 2
	v_sub_u32_e32 v116, 0, v116
	v_and_b32_e32 v116, 3, v116
	v_lshlrev_b32_e32 v116, 4, v116
	v_xor_b32_e32 v129, v129, v116
	v_bfe_u32 v116, v118, 4, 2
	v_lshlrev_b32_e32 v116, 3, v116
	v_bfe_u32 v117, v118, 2, 2
	v_add_u32_e32 v116, v116, v117
	v_lshlrev_b32_e32 v116, 8, v116
	v_lshrrev_b32_e32 v68, 6, v118
	v_lshrrev_b32_e32 v127, 4, v118
	v_xor_b32_e32 v68, v68, v127
	v_and_b32_e32 v68, 1, v68
	v_lshlrev_b32_e32 v68, 7, v68
	v_or_b32_e32 v116, v116, v68
	v_and_b32_e32 v68, 3, v118
	v_lshlrev_b32_e32 v68, 3, v68
	v_or_b32_e32 v116, v116, v68
	v_xor_b32_e32 v68, 0, v117
	v_lshl_or_b32 v127, v68, 5, v116
	v_xor_b32_e32 v68, 1, v117
	v_lshl_or_b32 v128, v68, 5, v116
	v_xor_b32_e32 v68, 2, v117
	v_lshl_or_b32 v130, v68, 5, v116
	v_xor_b32_e32 v68, 3, v117
	v_lshl_or_b32 v122, v68, 5, v116
	v_lshrrev_b32_e32 v116, 6, v118
	s_nop 1
	v_readfirstlane_b32 s98, v116
	s_nop 1
	s_lshl_b32 s99, s98, 12
	s_lshl_b32 s98, s98, 11
	s_barrier
; #define LAS __attribute__((address_space(3)))
; __device__ __forceinline__ s16x4 lds_tr(lds_cptr p) { return __builtin_bit_cast(s16x4, __builtin_amdgcn_ds_read_tr16_b64_v4i16((LAS s16x4*)p)); }
;     ...
;     auto compute = [&]() __attribute__((always_inline)) {
; #pragma unroll
;         for (int kh = 0; kh < 2; ++kh) {
;             bf16x8 af[4], bfr[4];
; #pragma unroll
;             for (int m = 0; m < 4; ++m) af[m] = *(const LAS bf16x8*)(la + kh * GA_KH + m * 1024);
; #pragma unroll
;             for (int n = 0; n < 4; ++n) {
;                 const s16x4 r0 = lds_tr(lb + kh * 32 * GB_ST + n * 32), r1 = lds_tr(lb + kh * 32 * GB_ST + n * 32 + bsw);
;                 bfr[n] = (bf16x8){r0[0], r0[1], r0[2], r0[3], r1[0], r1[1], r1[2], r1[3]};
;             }
; #pragma unroll
;             for (int m = 0; m < 4; ++m)
; #pragma unroll
;                 for (int n = 0; n < 4; ++n) acc[m][n] = __builtin_amdgcn_mfma_f32_16x16x32_bf16(bfr[n], af[m], acc[m][n], 0, 0, 0);
;         }
;     };
;     ...
;     gloadB(0, rb0); gloadA(0, ra0); gloadB(1, rb1);
;     for (int kt = 0; kt < nk; kt += 2) {
;         __syncthreads();
;         lstore(ra0, rb0);
;         __syncthreads();
;         gloadA(kt + 1, ra0);
;         if (kt + 2 < nk) gloadB(kt + 2, rb0);
;         compute();
;         __syncthreads();
;         lstore(ra0, rb1);
;         __syncthreads();
;         if (kt + 2 < nk) gloadA(kt + 2, ra0);
;         if (kt + 3 < nk) gloadB(kt + 3, rb1);
;         compute();
;     }
	s_add_u32 m0, s98, 0x0
	s_nop 0
	global_load_lds_dwordx4 v123, s[28:29]
	s_add_u32 m0, s98, 0x2040
	s_nop 0
	global_load_lds_dwordx4 v124, s[28:29]
	s_add_u32 m0, s98, 0x400
	s_nop 0
	global_load_lds_dwordx4 v125, s[28:29]
	s_add_u32 m0, s98, 0x2440
	s_nop 0
	global_load_lds_dwordx4 v126, s[28:29]
	s_add_u32 m0, s99, 0x4080
	s_nop 0
	global_load_lds_dwordx4 v214, s[44:45]
	s_add_u32 m0, s99, 0x4480
	s_nop 0
	global_load_lds_dwordx4 v215, s[44:45]
	s_add_u32 m0, s99, 0x4880
	s_nop 0
	global_load_lds_dwordx4 v216, s[44:45]
	s_add_u32 m0, s99, 0x4c80
	s_nop 0
	global_load_lds_dwordx4 v217, s[44:45]
	s_add_u32 s28, s28, 0x80
	s_addc_u32 s29, s29, 0
	s_add_u32 s44, s44, 0x20000
	s_addc_u32 s45, s45, 0
	s_mov_b32 s7, 0
	v_mov_b32_e32 v5, v4
	v_mov_b32_e32 v6, v4
	v_mov_b32_e32 v7, v4
	v_mov_b32_e32 v16, v4
	v_mov_b32_e32 v17, v4
	v_mov_b32_e32 v18, v4
	v_mov_b32_e32 v19, v4
	v_mov_b32_e32 v8, v4
	v_mov_b32_e32 v9, v4
	v_mov_b32_e32 v10, v4
	v_mov_b32_e32 v11, v4
	v_mov_b32_e32 v12, v4
	v_mov_b32_e32 v13, v4
	v_mov_b32_e32 v14, v4
	v_mov_b32_e32 v15, v4
	v_mov_b32_e32 v20, v4
	v_mov_b32_e32 v21, v4
	v_mov_b32_e32 v22, v4
	v_mov_b32_e32 v23, v4
	v_mov_b32_e32 v60, v4
	v_mov_b32_e32 v61, v4
	v_mov_b32_e32 v62, v4
	v_mov_b32_e32 v63, v4
	v_mov_b32_e32 v28, v4
	v_mov_b32_e32 v29, v4
	v_mov_b32_e32 v30, v4
	v_mov_b32_e32 v31, v4
	v_mov_b32_e32 v72, v4
	v_mov_b32_e32 v73, v4
	v_mov_b32_e32 v74, v4
	v_mov_b32_e32 v75, v4
	v_mov_b32_e32 v84, v4
	v_mov_b32_e32 v85, v4
	v_mov_b32_e32 v86, v4
	v_mov_b32_e32 v87, v4
	v_mov_b32_e32 v92, v4
	v_mov_b32_e32 v93, v4
	v_mov_b32_e32 v94, v4
	v_mov_b32_e32 v95, v4
	v_mov_b32_e32 v88, v4
	v_mov_b32_e32 v89, v4
	v_mov_b32_e32 v90, v4
	v_mov_b32_e32 v91, v4
	v_mov_b32_e32 v96, v4
	v_mov_b32_e32 v97, v4
	v_mov_b32_e32 v98, v4
	v_mov_b32_e32 v99, v4
	v_mov_b32_e32 v100, v4
	v_mov_b32_e32 v101, v4
	v_mov_b32_e32 v102, v4
	v_mov_b32_e32 v103, v4
	v_mov_b32_e32 v108, v4
	v_mov_b32_e32 v109, v4
	v_mov_b32_e32 v110, v4
	v_mov_b32_e32 v111, v4
	v_mov_b32_e32 v104, v4
	v_mov_b32_e32 v105, v4
	v_mov_b32_e32 v106, v4
	v_mov_b32_e32 v107, v4
	v_mov_b32_e32 v112, v4
	v_mov_b32_e32 v113, v4
	v_mov_b32_e32 v114, v4
	v_mov_b32_e32 v115, v4
	s_waitcnt vmcnt(0)
	s_barrier
.Lm1_loop:
	s_add_u32 m0, s98, 0x9000
	ds_read_b64_tr_b16 v[174:175], v127 offset:16512
	ds_read_b64_tr_b16 v[176:177], v127 offset:17536
	ds_read_b128 v[158:161], v129
	ds_read_b64_tr_b16 v[178:179], v128 offset:16512
	ds_read_b64_tr_b16 v[180:181], v128 offset:17536
	s_waitcnt lgkmcnt(2)
	v_mfma_f32_16x16x32_bf16 v[112:115], v[174:177], v[158:161], v[112:115]
	global_load_lds_dwordx4 v123, s[28:29]
	s_add_u32 m0, s98, 0xb040
	ds_read_b64_tr_b16 v[182:183], v130 offset:16512
	ds_read_b64_tr_b16 v[184:185], v130 offset:17536
	s_waitcnt lgkmcnt(2)
	v_mfma_f32_16x16x32_bf16 v[104:107], v[178:181], v[158:161], v[104:107]
	global_load_lds_dwordx4 v124, s[28:29]
	s_add_u32 m0, s98, 0x9400
	ds_read_b64_tr_b16 v[186:187], v122 offset:16512
	ds_read_b64_tr_b16 v[188:189], v122 offset:17536
	s_waitcnt lgkmcnt(2)
	v_mfma_f32_16x16x32_bf16 v[108:111], v[182:185], v[158:161], v[108:111]
	global_load_lds_dwordx4 v125, s[28:29]
	s_add_u32 m0, s98, 0xb440
	ds_read_b128 v[162:165], v129 offset:1024
	s_waitcnt lgkmcnt(1)
	v_mfma_f32_16x16x32_bf16 v[100:103], v[186:189], v[158:161], v[100:103]
	global_load_lds_dwordx4 v126, s[28:29]
	s_add_u32 m0, s99, 0xd080
	ds_read_b128 v[166:169], v129 offset:2048
	s_waitcnt lgkmcnt(1)
	v_mfma_f32_16x16x32_bf16 v[96:99], v[174:177], v[162:165], v[96:99]
	global_load_lds_dwordx4 v214, s[44:45]
	s_add_u32 m0, s99, 0xd480
	ds_read_b128 v[170:173], v129 offset:3072
	v_mfma_f32_16x16x32_bf16 v[88:91], v[178:181], v[162:165], v[88:91]
	global_load_lds_dwordx4 v215, s[44:45]
	s_add_u32 m0, s99, 0xd880
	ds_read_b64_tr_b16 v[190:191], v127 offset:24704
	ds_read_b64_tr_b16 v[192:193], v127 offset:25728
	v_mfma_f32_16x16x32_bf16 v[92:95], v[182:185], v[162:165], v[92:95]
	global_load_lds_dwordx4 v216, s[44:45]
	s_add_u32 m0, s99, 0xdc80
	ds_read_b64_tr_b16 v[132:133], v128 offset:24704
	ds_read_b64_tr_b16 v[134:135], v128 offset:25728
	v_mfma_f32_16x16x32_bf16 v[84:87], v[186:189], v[162:165], v[84:87]
	global_load_lds_dwordx4 v217, s[44:45]
	s_add_u32 s28, s28, 0x80
	s_addc_u32 s29, s29, 0
	s_add_u32 s44, s44, 0x20000
	s_addc_u32 s45, s45, 0
	ds_read_b128 v[158:161], v129 offset:8256
	s_waitcnt lgkmcnt(6)
	v_mfma_f32_16x16x32_bf16 v[72:75], v[174:177], v[166:169], v[72:75]
	ds_read_b64_tr_b16 v[136:137], v130 offset:24704
	ds_read_b64_tr_b16 v[138:139], v130 offset:25728
	v_mfma_f32_16x16x32_bf16 v[28:31], v[178:181], v[166:169], v[28:31]
	ds_read_b64_tr_b16 v[140:141], v122 offset:24704
	ds_read_b64_tr_b16 v[142:143], v122 offset:25728
	v_mfma_f32_16x16x32_bf16 v[60:63], v[182:185], v[166:169], v[60:63]
	v_mfma_f32_16x16x32_bf16 v[20:23], v[186:189], v[166:169], v[20:23]
	ds_read_b128 v[162:165], v129 offset:9280
	s_waitcnt lgkmcnt(10)
	v_mfma_f32_16x16x32_bf16 v[12:15], v[174:177], v[170:173], v[12:15]
	v_mfma_f32_16x16x32_bf16 v[8:11], v[178:181], v[170:173], v[8:11]
	v_mfma_f32_16x16x32_bf16 v[16:19], v[182:185], v[170:173], v[16:19]
	v_mfma_f32_16x16x32_bf16 v[4:7], v[186:189], v[170:173], v[4:7]
	ds_read_b128 v[166:169], v129 offset:10304
	s_waitcnt lgkmcnt(6)
	v_mfma_f32_16x16x32_bf16 v[112:115], v[190:193], v[158:161], v[112:115]
	v_mfma_f32_16x16x32_bf16 v[104:107], v[132:135], v[158:161], v[104:107]
	s_waitcnt lgkmcnt(4)
	v_mfma_f32_16x16x32_bf16 v[108:111], v[136:139], v[158:161], v[108:111]
	s_waitcnt lgkmcnt(2)
	v_mfma_f32_16x16x32_bf16 v[100:103], v[140:143], v[158:161], v[100:103]
	ds_read_b128 v[170:173], v129 offset:11328
	s_waitcnt lgkmcnt(2)
	v_mfma_f32_16x16x32_bf16 v[96:99], v[190:193], v[162:165], v[96:99]
	v_mfma_f32_16x16x32_bf16 v[88:91], v[132:135], v[162:165], v[88:91]
	v_mfma_f32_16x16x32_bf16 v[92:95], v[136:139], v[162:165], v[92:95]
	v_mfma_f32_16x16x32_bf16 v[84:87], v[140:143], v[162:165], v[84:87]
	s_waitcnt lgkmcnt(1)
	v_mfma_f32_16x16x32_bf16 v[72:75], v[190:193], v[166:169], v[72:75]
	v_mfma_f32_16x16x32_bf16 v[28:31], v[132:135], v[166:169], v[28:31]
	v_mfma_f32_16x16x32_bf16 v[60:63], v[136:139], v[166:169], v[60:63]
	v_mfma_f32_16x16x32_bf16 v[20:23], v[140:143], v[166:169], v[20:23]
	s_waitcnt lgkmcnt(0)
	v_mfma_f32_16x16x32_bf16 v[12:15], v[190:193], v[170:173], v[12:15]
	v_mfma_f32_16x16x32_bf16 v[8:11], v[132:135], v[170:173], v[8:11]
	v_mfma_f32_16x16x32_bf16 v[16:19], v[136:139], v[170:173], v[16:19]
	v_mfma_f32_16x16x32_bf16 v[4:7], v[140:143], v[170:173], v[4:7]
	s_waitcnt vmcnt(0) lgkmcnt(0)
	s_barrier
; #define LAS __attribute__((address_space(3)))
; __device__ __forceinline__ s16x4 lds_tr(lds_cptr p) { return __builtin_bit_cast(s16x4, __builtin_amdgcn_ds_read_tr16_b64_v4i16((LAS s16x4*)p)); }
;     ...
;     auto compute = [&]() __attribute__((always_inline)) {
; #pragma unroll
;         for (int kh = 0; kh < 2; ++kh) {
;             bf16x8 af[4], bfr[4];
; #pragma unroll
;             for (int m = 0; m < 4; ++m) af[m] = *(const LAS bf16x8*)(la + kh * GA_KH + m * 1024);
; #pragma unroll
;             for (int n = 0; n < 4; ++n) {
;                 const s16x4 r0 = lds_tr(lb + kh * 32 * GB_ST + n * 32), r1 = lds_tr(lb + kh * 32 * GB_ST + n * 32 + bsw);
;                 bfr[n] = (bf16x8){r0[0], r0[1], r0[2], r0[3], r1[0], r1[1], r1[2], r1[3]};
;             }
; #pragma unroll
;             for (int m = 0; m < 4; ++m)
; #pragma unroll
;                 for (int n = 0; n < 4; ++n) acc[m][n] = __builtin_amdgcn_mfma_f32_16x16x32_bf16(bfr[n], af[m], acc[m][n], 0, 0, 0);
;         }
;     };
;     ...
;     gloadB(0, rb0); gloadA(0, ra0); gloadB(1, rb1);
;     for (int kt = 0; kt < nk; kt += 2) {
;         __syncthreads();
;         lstore(ra0, rb0);
;         __syncthreads();
;         gloadA(kt + 1, ra0);
;         if (kt + 2 < nk) gloadB(kt + 2, rb0);
;         compute();
;         __syncthreads();
;         lstore(ra0, rb1);
;         __syncthreads();
;         if (kt + 2 < nk) gloadA(kt + 2, ra0);
;         if (kt + 3 < nk) gloadB(kt + 3, rb1);
;         compute();
;     }
	s_add_u32 m0, s98, 0x0
	ds_read_b64_tr_b16 v[174:175], v127 offset:53376
	ds_read_b64_tr_b16 v[176:177], v127 offset:54400
	ds_read_b128 v[158:161], v129 offset:36864
	ds_read_b64_tr_b16 v[178:179], v128 offset:53376
	ds_read_b64_tr_b16 v[180:181], v128 offset:54400
	s_waitcnt lgkmcnt(2)
	v_mfma_f32_16x16x32_bf16 v[112:115], v[174:177], v[158:161], v[112:115]
	global_load_lds_dwordx4 v123, s[28:29]
	s_add_u32 m0, s98, 0x2040
	ds_read_b64_tr_b16 v[182:183], v130 offset:53376
	ds_read_b64_tr_b16 v[184:185], v130 offset:54400
	s_waitcnt lgkmcnt(2)
	v_mfma_f32_16x16x32_bf16 v[104:107], v[178:181], v[158:161], v[104:107]
	global_load_lds_dwordx4 v124, s[28:29]
	s_add_u32 m0, s98, 0x400
	ds_read_b64_tr_b16 v[186:187], v122 offset:53376
	ds_read_b64_tr_b16 v[188:189], v122 offset:54400
	s_waitcnt lgkmcnt(2)
	v_mfma_f32_16x16x32_bf16 v[108:111], v[182:185], v[158:161], v[108:111]
	global_load_lds_dwordx4 v125, s[28:29]
	s_add_u32 m0, s98, 0x2440
	ds_read_b128 v[162:165], v129 offset:37888
	s_waitcnt lgkmcnt(1)
	v_mfma_f32_16x16x32_bf16 v[100:103], v[186:189], v[158:161], v[100:103]
	global_load_lds_dwordx4 v126, s[28:29]
	s_add_u32 m0, s99, 0x4080
	ds_read_b128 v[166:169], v129 offset:38912
	s_waitcnt lgkmcnt(1)
	v_mfma_f32_16x16x32_bf16 v[96:99], v[174:177], v[162:165], v[96:99]
	global_load_lds_dwordx4 v214, s[44:45]
	s_add_u32 m0, s99, 0x4480
	ds_read_b128 v[170:173], v129 offset:39936
	v_mfma_f32_16x16x32_bf16 v[88:91], v[178:181], v[162:165], v[88:91]
	global_load_lds_dwordx4 v215, s[44:45]
	s_add_u32 m0, s99, 0x4880
	ds_read_b64_tr_b16 v[190:191], v127 offset:61568
	ds_read_b64_tr_b16 v[192:193], v127 offset:62592
	v_mfma_f32_16x16x32_bf16 v[92:95], v[182:185], v[162:165], v[92:95]
	global_load_lds_dwordx4 v216, s[44:45]
	s_add_u32 m0, s99, 0x4c80
	ds_read_b64_tr_b16 v[132:133], v128 offset:61568
	ds_read_b64_tr_b16 v[134:135], v128 offset:62592
	v_mfma_f32_16x16x32_bf16 v[84:87], v[186:189], v[162:165], v[84:87]
	global_load_lds_dwordx4 v217, s[44:45]
	s_add_u32 s28, s28, 0x80
	s_addc_u32 s29, s29, 0
	s_add_u32 s44, s44, 0x20000
	s_addc_u32 s45, s45, 0
	ds_read_b128 v[158:161], v129 offset:45120
	s_waitcnt lgkmcnt(6)
	v_mfma_f32_16x16x32_bf16 v[72:75], v[174:177], v[166:169], v[72:75]
	ds_read_b64_tr_b16 v[136:137], v130 offset:61568
	ds_read_b64_tr_b16 v[138:139], v130 offset:62592
	v_mfma_f32_16x16x32_bf16 v[28:31], v[178:181], v[166:169], v[28:31]
	ds_read_b64_tr_b16 v[140:141], v122 offset:61568
	ds_read_b64_tr_b16 v[142:143], v122 offset:62592
	v_mfma_f32_16x16x32_bf16 v[60:63], v[182:185], v[166:169], v[60:63]
	v_mfma_f32_16x16x32_bf16 v[20:23], v[186:189], v[166:169], v[20:23]
	ds_read_b128 v[162:165], v129 offset:46144
	s_waitcnt lgkmcnt(10)
	v_mfma_f32_16x16x32_bf16 v[12:15], v[174:177], v[170:173], v[12:15]
	v_mfma_f32_16x16x32_bf16 v[8:11], v[178:181], v[170:173], v[8:11]
	v_mfma_f32_16x16x32_bf16 v[16:19], v[182:185], v[170:173], v[16:19]
	v_mfma_f32_16x16x32_bf16 v[4:7], v[186:189], v[170:173], v[4:7]
	ds_read_b128 v[166:169], v129 offset:47168
	s_waitcnt lgkmcnt(6)
	v_mfma_f32_16x16x32_bf16 v[112:115], v[190:193], v[158:161], v[112:115]
	v_mfma_f32_16x16x32_bf16 v[104:107], v[132:135], v[158:161], v[104:107]
	s_waitcnt lgkmcnt(4)
	v_mfma_f32_16x16x32_bf16 v[108:111], v[136:139], v[158:161], v[108:111]
	s_waitcnt lgkmcnt(2)
	v_mfma_f32_16x16x32_bf16 v[100:103], v[140:143], v[158:161], v[100:103]
	ds_read_b128 v[170:173], v129 offset:48192
	s_waitcnt lgkmcnt(2)
	v_mfma_f32_16x16x32_bf16 v[96:99], v[190:193], v[162:165], v[96:99]
	v_mfma_f32_16x16x32_bf16 v[88:91], v[132:135], v[162:165], v[88:91]
	v_mfma_f32_16x16x32_bf16 v[92:95], v[136:139], v[162:165], v[92:95]
	v_mfma_f32_16x16x32_bf16 v[84:87], v[140:143], v[162:165], v[84:87]
	s_waitcnt lgkmcnt(1)
	v_mfma_f32_16x16x32_bf16 v[72:75], v[190:193], v[166:169], v[72:75]
	v_mfma_f32_16x16x32_bf16 v[28:31], v[132:135], v[166:169], v[28:31]
	v_mfma_f32_16x16x32_bf16 v[60:63], v[136:139], v[166:169], v[60:63]
	v_mfma_f32_16x16x32_bf16 v[20:23], v[140:143], v[166:169], v[20:23]
	s_waitcnt lgkmcnt(0)
	v_mfma_f32_16x16x32_bf16 v[12:15], v[190:193], v[170:173], v[12:15]
	v_mfma_f32_16x16x32_bf16 v[8:11], v[132:135], v[170:173], v[8:11]
	v_mfma_f32_16x16x32_bf16 v[16:19], v[136:139], v[170:173], v[16:19]
	v_mfma_f32_16x16x32_bf16 v[4:7], v[140:143], v[170:173], v[4:7]
	s_waitcnt vmcnt(0) lgkmcnt(0)
	s_barrier
	s_add_i32 s7, s7, 2
	s_cmp_lt_u32 s7, 14
	s_cbranch_scc1 .Lm1_loop
; #define LAS __attribute__((address_space(3)))
; __device__ __forceinline__ s16x4 lds_tr(lds_cptr p) { return __builtin_bit_cast(s16x4, __builtin_amdgcn_ds_read_tr16_b64_v4i16((LAS s16x4*)p)); }
;     ...
;     auto compute = [&]() __attribute__((always_inline)) {
; #pragma unroll
;         for (int kh = 0; kh < 2; ++kh) {
;             bf16x8 af[4], bfr[4];
; #pragma unroll
;             for (int m = 0; m < 4; ++m) af[m] = *(const LAS bf16x8*)(la + kh * GA_KH + m * 1024);
; #pragma unroll
;             for (int n = 0; n < 4; ++n) {
;                 const s16x4 r0 = lds_tr(lb + kh * 32 * GB_ST + n * 32), r1 = lds_tr(lb + kh * 32 * GB_ST + n * 32 + bsw);
;                 bfr[n] = (bf16x8){r0[0], r0[1], r0[2], r0[3], r1[0], r1[1], r1[2], r1[3]};
;             }
; #pragma unroll
;             for (int m = 0; m < 4; ++m)
; #pragma unroll
;                 for (int n = 0; n < 4; ++n) acc[m][n] = __builtin_amdgcn_mfma_f32_16x16x32_bf16(bfr[n], af[m], acc[m][n], 0, 0, 0);
;         }
;     };
;     ...
;     gloadB(0, rb0); gloadA(0, ra0); gloadB(1, rb1);
;     for (int kt = 0; kt < nk; kt += 2) {
;         __syncthreads();
;         lstore(ra0, rb0);
;         __syncthreads();
;         gloadA(kt + 1, ra0);
;         if (kt + 2 < nk) gloadB(kt + 2, rb0);
;         compute();
;         __syncthreads();
;         lstore(ra0, rb1);
;         __syncthreads();
;         if (kt + 2 < nk) gloadA(kt + 2, ra0);
;         if (kt + 3 < nk) gloadB(kt + 3, rb1);
;         compute();
;     }
	s_add_u32 m0, s98, 0x9000
	ds_read_b64_tr_b16 v[174:175], v127 offset:16512
	ds_read_b64_tr_b16 v[176:177], v127 offset:17536
	ds_read_b128 v[158:161], v129
	ds_read_b64_tr_b16 v[178:179], v128 offset:16512
	ds_read_b64_tr_b16 v[180:181], v128 offset:17536
	s_waitcnt lgkmcnt(2)
	v_mfma_f32_16x16x32_bf16 v[112:115], v[174:177], v[158:161], v[112:115]
	global_load_lds_dwordx4 v123, s[28:29]
	s_add_u32 m0, s98, 0xb040
	ds_read_b64_tr_b16 v[182:183], v130 offset:16512
	ds_read_b64_tr_b16 v[184:185], v130 offset:17536
	s_waitcnt lgkmcnt(2)
	v_mfma_f32_16x16x32_bf16 v[104:107], v[178:181], v[158:161], v[104:107]
	global_load_lds_dwordx4 v124, s[28:29]
	s_add_u32 m0, s98, 0x9400
	ds_read_b64_tr_b16 v[186:187], v122 offset:16512
	ds_read_b64_tr_b16 v[188:189], v122 offset:17536
	s_waitcnt lgkmcnt(2)
	v_mfma_f32_16x16x32_bf16 v[108:111], v[182:185], v[158:161], v[108:111]
	global_load_lds_dwordx4 v125, s[28:29]
	s_add_u32 m0, s98, 0xb440
	ds_read_b128 v[162:165], v129 offset:1024
	s_waitcnt lgkmcnt(1)
	v_mfma_f32_16x16x32_bf16 v[100:103], v[186:189], v[158:161], v[100:103]
	global_load_lds_dwordx4 v126, s[28:29]
	s_add_u32 m0, s99, 0xd080
	ds_read_b128 v[166:169], v129 offset:2048
	s_waitcnt lgkmcnt(1)
	v_mfma_f32_16x16x32_bf16 v[96:99], v[174:177], v[162:165], v[96:99]
	global_load_lds_dwordx4 v214, s[44:45]
	s_add_u32 m0, s99, 0xd480
	ds_read_b128 v[170:173], v129 offset:3072
	v_mfma_f32_16x16x32_bf16 v[88:91], v[178:181], v[162:165], v[88:91]
	global_load_lds_dwordx4 v215, s[44:45]
	s_add_u32 m0, s99, 0xd880
	ds_read_b64_tr_b16 v[190:191], v127 offset:24704
	ds_read_b64_tr_b16 v[192:193], v127 offset:25728
	v_mfma_f32_16x16x32_bf16 v[92:95], v[182:185], v[162:165], v[92:95]
	global_load_lds_dwordx4 v216, s[44:45]
	s_add_u32 m0, s99, 0xdc80
	ds_read_b64_tr_b16 v[132:133], v128 offset:24704
	ds_read_b64_tr_b16 v[134:135], v128 offset:25728
	v_mfma_f32_16x16x32_bf16 v[84:87], v[186:189], v[162:165], v[84:87]
	global_load_lds_dwordx4 v217, s[44:45]
	s_add_u32 s28, s28, 0x80
	s_addc_u32 s29, s29, 0
	s_add_u32 s44, s44, 0x20000
	s_addc_u32 s45, s45, 0
	ds_read_b128 v[158:161], v129 offset:8256
	s_waitcnt lgkmcnt(6)
	v_mfma_f32_16x16x32_bf16 v[72:75], v[174:177], v[166:169], v[72:75]
	ds_read_b64_tr_b16 v[136:137], v130 offset:24704
	ds_read_b64_tr_b16 v[138:139], v130 offset:25728
	v_mfma_f32_16x16x32_bf16 v[28:31], v[178:181], v[166:169], v[28:31]
	ds_read_b64_tr_b16 v[140:141], v122 offset:24704
	ds_read_b64_tr_b16 v[142:143], v122 offset:25728
	v_mfma_f32_16x16x32_bf16 v[60:63], v[182:185], v[166:169], v[60:63]
	v_mfma_f32_16x16x32_bf16 v[20:23], v[186:189], v[166:169], v[20:23]
	ds_read_b128 v[162:165], v129 offset:9280
	s_waitcnt lgkmcnt(10)
	v_mfma_f32_16x16x32_bf16 v[12:15], v[174:177], v[170:173], v[12:15]
	v_mfma_f32_16x16x32_bf16 v[8:11], v[178:181], v[170:173], v[8:11]
	v_mfma_f32_16x16x32_bf16 v[16:19], v[182:185], v[170:173], v[16:19]
	v_mfma_f32_16x16x32_bf16 v[4:7], v[186:189], v[170:173], v[4:7]
	ds_read_b128 v[166:169], v129 offset:10304
	s_waitcnt lgkmcnt(6)
	v_mfma_f32_16x16x32_bf16 v[112:115], v[190:193], v[158:161], v[112:115]
	v_mfma_f32_16x16x32_bf16 v[104:107], v[132:135], v[158:161], v[104:107]
	s_waitcnt lgkmcnt(4)
	v_mfma_f32_16x16x32_bf16 v[108:111], v[136:139], v[158:161], v[108:111]
	s_waitcnt lgkmcnt(2)
	v_mfma_f32_16x16x32_bf16 v[100:103], v[140:143], v[158:161], v[100:103]
	ds_read_b128 v[170:173], v129 offset:11328
	s_waitcnt lgkmcnt(2)
	v_mfma_f32_16x16x32_bf16 v[96:99], v[190:193], v[162:165], v[96:99]
	v_mfma_f32_16x16x32_bf16 v[88:91], v[132:135], v[162:165], v[88:91]
	v_mfma_f32_16x16x32_bf16 v[92:95], v[136:139], v[162:165], v[92:95]
	v_mfma_f32_16x16x32_bf16 v[84:87], v[140:143], v[162:165], v[84:87]
	s_waitcnt lgkmcnt(1)
	v_mfma_f32_16x16x32_bf16 v[72:75], v[190:193], v[166:169], v[72:75]
	v_mfma_f32_16x16x32_bf16 v[28:31], v[132:135], v[166:169], v[28:31]
	v_mfma_f32_16x16x32_bf16 v[60:63], v[136:139], v[166:169], v[60:63]
	v_mfma_f32_16x16x32_bf16 v[20:23], v[140:143], v[166:169], v[20:23]
	s_waitcnt lgkmcnt(0)
	v_mfma_f32_16x16x32_bf16 v[12:15], v[190:193], v[170:173], v[12:15]
	v_mfma_f32_16x16x32_bf16 v[8:11], v[132:135], v[170:173], v[8:11]
	v_mfma_f32_16x16x32_bf16 v[16:19], v[136:139], v[170:173], v[16:19]
	v_mfma_f32_16x16x32_bf16 v[4:7], v[140:143], v[170:173], v[4:7]
	s_waitcnt vmcnt(0) lgkmcnt(0)
	s_barrier
; #define LAS __attribute__((address_space(3)))
; __device__ __forceinline__ s16x4 lds_tr(lds_cptr p) { return __builtin_bit_cast(s16x4, __builtin_amdgcn_ds_read_tr16_b64_v4i16((LAS s16x4*)p)); }
;     ...
;     auto compute = [&]() __attribute__((always_inline)) {
; #pragma unroll
;         for (int kh = 0; kh < 2; ++kh) {
;             bf16x8 af[4], bfr[4];
; #pragma unroll
;             for (int m = 0; m < 4; ++m) af[m] = *(const LAS bf16x8*)(la + kh * GA_KH + m * 1024);
; #pragma unroll
;             for (int n = 0; n < 4; ++n) {
;                 const s16x4 r0 = lds_tr(lb + kh * 32 * GB_ST + n * 32), r1 = lds_tr(lb + kh * 32 * GB_ST + n * 32 + bsw);
;                 bfr[n] = (bf16x8){r0[0], r0[1], r0[2], r0[3], r1[0], r1[1], r1[2], r1[3]};
;             }
; #pragma unroll
;             for (int m = 0; m < 4; ++m)
; #pragma unroll
;                 for (int n = 0; n < 4; ++n) acc[m][n] = __builtin_amdgcn_mfma_f32_16x16x32_bf16(bfr[n], af[m], acc[m][n], 0, 0, 0);
;         }
;     };
;     ...
;     gloadB(0, rb0); gloadA(0, ra0); gloadB(1, rb1);
;     for (int kt = 0; kt < nk; kt += 2) {
;         __syncthreads();
;         lstore(ra0, rb0);
;         __syncthreads();
;         gloadA(kt + 1, ra0);
;         if (kt + 2 < nk) gloadB(kt + 2, rb0);
;         compute();
;         __syncthreads();
;         lstore(ra0, rb1);
;         __syncthreads();
;         if (kt + 2 < nk) gloadA(kt + 2, ra0);
;         if (kt + 3 < nk) gloadB(kt + 3, rb1);
;         compute();
;     }
	ds_read_b64_tr_b16 v[174:175], v127 offset:53376
	ds_read_b64_tr_b16 v[176:177], v127 offset:54400
	ds_read_b128 v[158:161], v129 offset:36864
	ds_read_b64_tr_b16 v[178:179], v128 offset:53376
	ds_read_b64_tr_b16 v[180:181], v128 offset:54400
	s_waitcnt lgkmcnt(2)
	v_mfma_f32_16x16x32_bf16 v[112:115], v[174:177], v[158:161], v[112:115]
	ds_read_b64_tr_b16 v[182:183], v130 offset:53376
	ds_read_b64_tr_b16 v[184:185], v130 offset:54400
	s_waitcnt lgkmcnt(2)
	v_mfma_f32_16x16x32_bf16 v[104:107], v[178:181], v[158:161], v[104:107]
	ds_read_b64_tr_b16 v[186:187], v122 offset:53376
	ds_read_b64_tr_b16 v[188:189], v122 offset:54400
	s_waitcnt lgkmcnt(2)
	v_mfma_f32_16x16x32_bf16 v[108:111], v[182:185], v[158:161], v[108:111]
	ds_read_b128 v[162:165], v129 offset:37888
	s_waitcnt lgkmcnt(1)
	v_mfma_f32_16x16x32_bf16 v[100:103], v[186:189], v[158:161], v[100:103]
	ds_read_b128 v[166:169], v129 offset:38912
	s_waitcnt lgkmcnt(1)
	v_mfma_f32_16x16x32_bf16 v[96:99], v[174:177], v[162:165], v[96:99]
	ds_read_b128 v[170:173], v129 offset:39936
	v_mfma_f32_16x16x32_bf16 v[88:91], v[178:181], v[162:165], v[88:91]
	ds_read_b64_tr_b16 v[190:191], v127 offset:61568
	ds_read_b64_tr_b16 v[192:193], v127 offset:62592
	v_mfma_f32_16x16x32_bf16 v[92:95], v[182:185], v[162:165], v[92:95]
	ds_read_b64_tr_b16 v[132:133], v128 offset:61568
	ds_read_b64_tr_b16 v[134:135], v128 offset:62592
	v_mfma_f32_16x16x32_bf16 v[84:87], v[186:189], v[162:165], v[84:87]
	ds_read_b128 v[158:161], v129 offset:45120
	s_waitcnt lgkmcnt(6)
	v_mfma_f32_16x16x32_bf16 v[72:75], v[174:177], v[166:169], v[72:75]
	ds_read_b64_tr_b16 v[136:137], v130 offset:61568
	ds_read_b64_tr_b16 v[138:139], v130 offset:62592
	v_mfma_f32_16x16x32_bf16 v[28:31], v[178:181], v[166:169], v[28:31]
	ds_read_b64_tr_b16 v[140:141], v122 offset:61568
	ds_read_b64_tr_b16 v[142:143], v122 offset:62592
	v_mfma_f32_16x16x32_bf16 v[60:63], v[182:185], v[166:169], v[60:63]
	v_mfma_f32_16x16x32_bf16 v[20:23], v[186:189], v[166:169], v[20:23]
	ds_read_b128 v[162:165], v129 offset:46144
	s_waitcnt lgkmcnt(10)
	v_mfma_f32_16x16x32_bf16 v[12:15], v[174:177], v[170:173], v[12:15]
	v_mfma_f32_16x16x32_bf16 v[8:11], v[178:181], v[170:173], v[8:11]
	v_mfma_f32_16x16x32_bf16 v[16:19], v[182:185], v[170:173], v[16:19]
	v_mfma_f32_16x16x32_bf16 v[4:7], v[186:189], v[170:173], v[4:7]
	ds_read_b128 v[166:169], v129 offset:47168
	s_waitcnt lgkmcnt(6)
	v_mfma_f32_16x16x32_bf16 v[112:115], v[190:193], v[158:161], v[112:115]
	v_mfma_f32_16x16x32_bf16 v[104:107], v[132:135], v[158:161], v[104:107]
	s_waitcnt lgkmcnt(4)
	v_mfma_f32_16x16x32_bf16 v[108:111], v[136:139], v[158:161], v[108:111]
	s_waitcnt lgkmcnt(2)
	v_mfma_f32_16x16x32_bf16 v[100:103], v[140:143], v[158:161], v[100:103]
	ds_read_b128 v[170:173], v129 offset:48192
	s_waitcnt lgkmcnt(2)
	v_mfma_f32_16x16x32_bf16 v[96:99], v[190:193], v[162:165], v[96:99]
	v_mfma_f32_16x16x32_bf16 v[88:91], v[132:135], v[162:165], v[88:91]
	v_mfma_f32_16x16x32_bf16 v[92:95], v[136:139], v[162:165], v[92:95]
	v_mfma_f32_16x16x32_bf16 v[84:87], v[140:143], v[162:165], v[84:87]
	s_waitcnt lgkmcnt(1)
	v_mfma_f32_16x16x32_bf16 v[72:75], v[190:193], v[166:169], v[72:75]
	v_mfma_f32_16x16x32_bf16 v[28:31], v[132:135], v[166:169], v[28:31]
	v_mfma_f32_16x16x32_bf16 v[60:63], v[136:139], v[166:169], v[60:63]
	v_mfma_f32_16x16x32_bf16 v[20:23], v[140:143], v[166:169], v[20:23]
	s_waitcnt lgkmcnt(0)
	v_mfma_f32_16x16x32_bf16 v[12:15], v[190:193], v[170:173], v[12:15]
	v_mfma_f32_16x16x32_bf16 v[8:11], v[132:135], v[170:173], v[8:11]
	v_mfma_f32_16x16x32_bf16 v[16:19], v[136:139], v[170:173], v[16:19]
	v_mfma_f32_16x16x32_bf16 v[4:7], v[140:143], v[170:173], v[4:7]
	s_waitcnt vmcnt(0) lgkmcnt(0)
	s_barrier
